# indexer query-fragment staging: the four per-thread row loads issued together; sparse bias-bucket table build: four LDS byte reads issued together with v_cndmask instead of four exec-branched reads
# speedup vs baseline: 1.0210x; 1.0021x over previous
.LBB0_369:
	s_or_b64 exec, exec, s[0:1]
	s_ashr_i32 s92, s18, 8
	s_and_b32 s81, s18, 0xff
	s_ashr_i32 s93, s92, 31
	s_lshl_b32 s89, s81, 5
	s_lshl_b64 s[90:91], s[92:93], 13
	s_and_saveexec_b64 s[16:17], s[52:53]
	s_cbranch_execz .LBB0_376
	v_or_b32_e32 v2, s89, v218
	v_or_b32_e32 v2, s90, v2
	s_waitcnt vmcnt(1)
	v_mov_b64_e32 v[4:5], s[44:45]
	s_movk_i32 s0, 0xe00
	v_mad_u64_u32 v[16:17], s[0:1], v2, s0, v[4:5]
	v_mad_i32_i24 v17, s91, v240, v17
	s_mov_b64 s[22:23], 0
	v_lshl_add_u32 v18, v0, 4, 0
	v_mov_b32_e32 v19, v0
	v_ashrrev_i32_e32 v9, 8, v19
	v_bfe_u32 v2, v19, 6, 2
	v_bfe_u32 v4, v19, 5, 1
	v_lshlrev_b32_e32 v2, 5, v2
	v_lshlrev_b32_e32 v8, 4, v4
	v_lshlrev_b32_e32 v4, 6, v9
	v_ashrrev_i32_e32 v5, 31, v4
	v_lshl_add_u64 v[4:5], v[4:5], 1, v[16:17]
	v_lshl_add_u64 v[4:5], v[4:5], 0, v[2:3]
	v_mov_b32_e32 v9, v3
	v_lshl_add_u64 v[12:13], v[4:5], 0, v[8:9]
	global_load_dwordx4 v[4:7], v[12:13], off offset:2304
	global_load_dwordx4 v[36:39], v[12:13], off offset:2560
	global_load_dwordx4 v[40:43], v[12:13], off offset:2816
	global_load_dwordx4 v[44:47], v[12:13], off offset:3072
	s_waitcnt vmcnt(3)
	ds_write_b128 v18, v[4:7]
	s_waitcnt vmcnt(2)
	ds_write_b128 v18, v[36:39] offset:8192
	s_waitcnt vmcnt(1)
	ds_write_b128 v18, v[40:43] offset:16384
	s_waitcnt vmcnt(0)
	ds_write_b128 v18, v[44:47] offset:24576
	v_add_u32_e32 v18, 0x8000, v18
	v_add_u32_e32 v19, 0x800, v19
	s_movk_i32 s0, 0x8ff
	v_cmp_lt_i32_e32 vcc, s0, v19
	s_or_b64 s[22:23], vcc, s[22:23]
	s_andn2_b64 exec, exec, s[22:23]
	s_cbranch_execz .LBB0_376
	s_branch .LBB0_372

.LBB0_1373:
	s_mov_b64 s[28:29], 0
	s_and_b64 vcc, exec, s[18:19]
	s_mov_b64 s[30:31], 0
	s_cbranch_vccz .LBB0_1383
	ds_read_u8 v160, v247
	ds_read_u8 v161, v248
	ds_read_u8 v162, v249
	ds_read_u8 v163, v250
	v_mov_b32_e32 v2, 0x800
	s_waitcnt lgkmcnt(0)
	v_lshlrev_b32_e32 v160, 6, v160
	v_lshlrev_b32_e32 v161, 6, v161
	v_lshlrev_b32_e32 v162, 6, v162
	v_lshlrev_b32_e32 v163, 6, v163
	v_cndmask_b32_e64 v160, v2, v160, s[8:9]
	v_cndmask_b32_e64 v161, v2, v161, s[10:11]
	v_cndmask_b32_e64 v162, v2, v162, s[12:13]
	v_cndmask_b32_e64 v163, v2, v163, s[14:15]
	ds_write_b128 v242, v[140:143] offset:10496
	ds_write_b128 v242, v[160:163] offset:11520
	s_waitcnt lgkmcnt(0)
	v_add_u32_e32 v170, 0x2800, v243
	ds_read2_b32 v[162:163], v170 offset0:64 offset1:80
	ds_read2_b32 v[166:167], v170 offset0:96 offset1:112
	ds_read2_b32 v[168:169], v170 offset0:128 offset1:144
	ds_read2_b32 v[170:171], v170 offset0:160 offset1:176
	v_add_u32_e32 v186, 0x2800, v244
	s_waitcnt lgkmcnt(3)
	v_add_u32_e32 v160, v162, v208
	v_add_u32_e32 v162, v163, v208
	s_waitcnt lgkmcnt(2)
	v_add_u32_e32 v164, v166, v208
	v_add_u32_e32 v166, v167, v208
	s_waitcnt lgkmcnt(1)
	v_add_u32_e32 v178, v168, v208
	v_add_u32_e32 v180, v169, v208
	ds_read2_b32 v[168:169], v186 offset0:64 offset1:80
	s_waitcnt lgkmcnt(1)
	v_add_u32_e32 v182, v170, v208
	v_add_u32_e32 v184, v171, v208
	ds_read2_b32 v[170:171], v186 offset0:96 offset1:112
	s_waitcnt lgkmcnt(1)
	v_add_u32_e32 v186, v168, v209
	ds_read_b32 v168, v244 offset:10752
	v_add_u32_e32 v188, v169, v209
	s_waitcnt lgkmcnt(1)
	v_add_u32_e32 v190, v170, v209
	v_add_u32_e32 v192, v171, v209
	s_waitcnt lgkmcnt(0)
	v_add_u32_e32 v194, v168, v209
	s_mov_b64 s[30:31], -1
